# scan pass 1: static s_setprio 1 for waves 0-3 (the other half than the previous priority test) for the duration of the stage
# speedup vs baseline: 1.0026x; 1.0026x over previous
.LBB0_346:
	s_or_b64 exec, exec, s[0:1]
	s_mov_b64 s[0:1], s[46:47]
	v_mov_b32_e32 v66, v186
	s_waitcnt lgkmcnt(0)
	s_barrier
	s_load_dwordx2 s[2:3], s[0:1], 0x98
	v_readlane_b32 s0, v235, 16
	s_cmpk_lt_i32 s0, 0x140
	v_readlane_b32 s1, v235, 17
	s_cbranch_scc0 .LBB0_368
	v_readfirstlane_b32 s99, v186
	s_nop 0
	s_lshr_b32 s99, s99, 6
	s_cmp_ge_u32 s99, 4
	s_cbranch_scc1 .Lscan_prio_done
	s_setprio 1
